# S6 + tile-expert word and source rows reused while the row tile repeats (13 of 14 units): the unit header issues no load then
# baseline (speedup 1.0000x reference)
.LBB0_1296:
	v_readlane_b32 s0, v253, 2
	v_readlane_b32 s1, v253, 3
	s_load_dwordx2 s[0:1], s[0:1], 0xf8
	v_readlane_b32 s20, v253, 6
	v_readlane_b32 s22, v253, 8
	v_readlane_b32 s23, v253, 9
	s_mov_b64 s[10:11], s[22:23]
	s_waitcnt lgkmcnt(0)
	global_load_dword v0, v189, s[0:1] offset:512 sc1
	v_readlane_b32 s0, v255, 47
	s_add_i32 s2, s0, 10
	s_cmp_lt_i32 s2, s11
	v_mov_b32_e32 v1, 0x108
	s_cselect_b64 s[0:1], -1, 0
	s_cmp_gt_i32 s10, s3
	v_readlane_b32 s21, v253, 7
	s_waitcnt vmcnt(0)
	v_readfirstlane_b32 s3, v0
	v_med3_i32 v0, v0, 0, v1
	s_nop 0
	v_readfirstlane_b32 s27, v0
	s_cbranch_scc1 .LBB0_1372
	s_cmp_gt_i32 s3, 0
	s_cselect_b64 s[10:11], -1, 0
	s_and_b64 s[10:11], s[16:17], s[10:11]
	s_andn2_b64 vcc, exec, s[10:11]
	s_cbranch_vccnz .LBB0_1316
	v_readlane_b32 s10, v253, 2
	v_readlane_b32 s11, v253, 3
	s_load_dwordx2 s[16:17], s[10:11], 0xf8
	v_mov_b32_e32 v0, 0x1000
	s_mul_i32 s13, s27, 56
	v_readlane_b32 s10, v255, 14
	s_waitcnt lgkmcnt(0)
	global_load_dword v1, v0, s[16:17] offset:24 sc1
	global_load_dword v2, v0, s[16:17] offset:28 sc1
	global_load_dwordx2 v[4:5], v0, s[16:17] offset:80 sc1
	v_mbcnt_lo_u32_b32 v0, -1, 0
	v_mbcnt_hi_u32_b32 v0, -1, v0
	s_cmp_ge_i32 s10, s13
	v_or_b32_e32 v0, s33, v0
	v_readlane_b32 s11, v255, 15
	v_readfirstlane_b32 s9, v0
	s_waitcnt vmcnt(0)
	v_readfirstlane_b32 s40, v4
	v_readfirstlane_b32 s41, v5
	s_cbranch_scc1 .LBB0_1316
	v_bfe_i32 v5, v0, 27, 1
	v_lshlrev_b32_e32 v3, 4, v0
	v_lshrrev_b32_e32 v5, 22, v5
	v_add_u32_e32 v5, v3, v5
	v_and_b32_e32 v5, 0xfffffc00, v5
	v_sub_u32_e32 v5, v3, v5
	v_ashrrev_i32_e32 v4, 31, v0
	v_lshrrev_b32_e32 v6, 4, v5
	v_lshrrev_b32_e32 v4, 26, v4
	v_bitop3_b32 v6, v6, v5, 32 bitop3:0x6c
	v_ashrrev_i32_e32 v5, 31, v5
	v_add_u32_e32 v4, v0, v4
	v_lshrrev_b32_e32 v5, 26, v5
	v_ashrrev_i32_e32 v4, 6, v4
	v_add_u32_e32 v5, v6, v5
	v_lshlrev_b32_e32 v7, 3, v4
	v_ashrrev_i32_e32 v5, 6, v5
	v_and_b32_e32 v7, -16, v7
	v_mul_i32_i24_e32 v8, 64, v5
	v_add_u32_e32 v7, v5, v7
	v_sub_u32_e32 v6, v6, v8
	v_lshlrev_b32_e32 v4, 5, v4
	v_ashrrev_i16_sdwa v6, v242, sext(v6) dst_sel:DWORD dst_unused:UNUSED_PAD src0_sel:DWORD src1_sel:BYTE_0
	v_lshlrev_b32_e32 v8, 1, v7
	v_lshrrev_b32_e32 v9, 2, v7
	v_and_b32_e32 v5, 3, v5
	s_mov_b32 s11, 0x1fffe0
	v_and_b32_e32 v4, 32, v4
	v_bfe_i32 v6, v6, 0, 16
	v_and_b32_e32 v8, 24, v8
	v_and_b32_e32 v9, 4, v9
	v_and_or_b32 v5, v7, s11, v5
	v_or3_b32 v5, v5, v9, v8
	v_add_lshl_u32 v4, v4, v6, 1
	v_add_u32_e32 v3, 0x2000, v3
	v_lshl_add_u32 v132, v7, 11, v4
	v_lshl_add_u32 v133, v5, 11, v4
	v_ashrrev_i32_e32 v4, 31, v3
	v_lshrrev_b32_e32 v4, 22, v4
	v_add_u32_e32 v4, v3, v4
	v_ashrrev_i32_e32 v4, 10, v4
	v_mul_i32_i24_e32 v5, 0x400, v4
	v_sub_u32_e32 v3, v3, v5
	v_lshrrev_b32_e32 v5, 4, v3
	v_bitop3_b32 v3, v5, v3, 32 bitop3:0x6c
	v_ashrrev_i32_e32 v6, 31, v3
	v_lshrrev_b32_e32 v6, 26, v6
	s_add_u32 s18, s16, 0x45900000
	v_lshlrev_b32_e32 v5, 3, v4
	v_add_u32_e32 v6, v3, v6
	v_writelane_b32 v255, s28, 48
	s_addc_u32 s19, s17, 0
	v_and_b32_e32 v5, -16, v5
	v_ashrrev_i32_e32 v7, 6, v6
	v_writelane_b32 v255, s29, 49
	s_add_u32 s28, s16, 0xb900000
	v_add_u32_e32 v5, v7, v5
	v_and_b32_e32 v7, 3, v7
	s_addc_u32 s29, s17, 0
	v_and_or_b32 v7, v5, s11, v7
	s_ashr_i32 s11, s9, 6
	s_lshr_b32 s30, s13, 3
	v_readlane_b32 s20, v254, 54
	s_ashr_i32 s10, s9, 8
	s_lshl_b32 s12, s11, 10
	s_add_i32 s31, s30, 1
	v_readlane_b32 s21, v254, 55
	s_and_b64 s[20:21], s[20:21], exec
	s_cselect_b32 s20, s31, s30
	v_readlane_b32 s21, v255, 0
	s_mul_i32 s20, s20, s21
	v_readlane_b32 s21, v255, 3
	s_add_i32 s20, s20, s21
	s_mul_hi_i32 s21, s20, 0x92492493
	s_add_i32 s21, s21, s20
	s_lshr_b32 s22, s21, 31
	s_ashr_i32 s21, s21, 8
	s_add_i32 s21, s21, s22
	v_and_b32_e32 v6, 0xc0, v6
	s_lshl_b32 s22, s21, 3
	v_sub_u32_e32 v3, v3, v6
	s_sub_i32 s23, s27, s22
	v_lshlrev_b32_e32 v4, 5, v4
	v_ashrrev_i16_sdwa v3, v242, sext(v3) dst_sel:DWORD dst_unused:UNUSED_PAD src0_sel:DWORD src1_sel:BYTE_0
	s_min_i32 s23, s23, 8
	s_mulk_i32 s21, 0x1c0
	v_and_b32_e32 v4, 32, v4
	v_bfe_i32 v3, v3, 0, 16
	s_sub_i32 s34, s20, s21
	s_sext_i32_i16 s20, s23
	v_add_lshl_u32 v3, v4, v3, 1
	v_cvt_f32_i32_e32 v4, s20
	v_lshlrev_b32_e32 v6, 1, v5
	v_lshrrev_b32_e32 v8, 2, v5
	v_and_b32_e32 v6, 24, v6
	v_and_b32_e32 v8, 4, v8
	v_or3_b32 v6, v7, v8, v6
	v_lshl_add_u32 v134, v5, 11, v3
	v_lshrrev_b32_e32 v232, 9, v132
	v_and_b32_e32 v232, -4, v232
	v_lshrrev_b32_e32 v233, 9, v134
	v_and_b32_e32 v233, -4, v233
	v_and_b32_e32 v234, 0x7ff, v132
	v_add_u32_e32 v234, 0x19900000, v234
	v_and_b32_e32 v235, 0x7ff, v134
	v_add_u32_e32 v235, 0x19900000, v235
	v_lshl_add_u32 v135, v6, 11, v3
	v_cvt_f32_i32_e32 v3, s34
	v_rcp_iflag_f32_e32 v5, v4
	s_xor_b32 s21, s34, s20
	s_ashr_i32 s21, s21, 30
	s_or_b32 s35, s21, 1
	v_mul_f32_e32 v5, v3, v5
	v_trunc_f32_e32 v5, v5
	v_fma_f32 v3, -v5, v4, v3
	v_cvt_i32_f32_e32 v5, v5
	v_cmp_ge_f32_e64 s[20:21], |v3|, |v4|
	s_and_b64 s[20:21], s[20:21], exec
	s_cselect_b32 s20, s35, 0
	v_readfirstlane_b32 s21, v5
	s_add_i32 s20, s21, s20
	s_sext_i32_i16 s85, s20
	s_mul_i32 s20, s20, s23
	s_sub_i32 s20, s34, s20
	s_sext_i32_i16 s20, s20
	s_add_i32 s52, s22, s20
	s_ashr_i32 s53, s52, 31
	s_lshl_b64 s[20:21], s[52:53], 2
	s_add_u32 s20, s16, s20
	s_addc_u32 s21, s17, s21
	global_load_dword v3, v189, s[20:21] offset:768
	s_lshl_b32 s92, s52, 10
	s_add_u32 s20, s18, s92
	s_addc_u32 s21, s19, 0
	global_load_dword v220, v232, s[20:21]
	global_load_dword v221, v233, s[20:21]
	global_load_dword v222, v232, s[20:21] offset:512
	global_load_dword v223, v233, s[20:21] offset:512
	s_lshl_b64 s[22:23], s[52:53], 19
	s_waitcnt vmcnt(0)
	s_lshl_b32 s92, s52, 19
	v_lshl_add_u32 v220, v220, 11, v234
	v_lshl_add_u32 v221, v221, 11, v235
	v_lshl_add_u32 v222, v222, 11, v234
	v_lshl_add_u32 v223, v223, 11, v235
	v_subrev_u32_e32 v220, s92, v220
	v_subrev_u32_e32 v221, s92, v221
	s_add_i32 s92, s92, 0x40000
	v_subrev_u32_e32 v222, s92, v222
	v_subrev_u32_e32 v223, s92, v223
	v_mov_b32_e32 v224, v220
	v_mov_b32_e32 v225, v221
	v_mov_b32_e32 v226, v222
	v_mov_b32_e32 v227, v223
	v_readfirstlane_b32 s20, v3
	s_mul_i32 s20, s20, 56
	s_mov_b32 s94, s20
	s_add_i32 s20, s20, s85
	s_ashr_i32 s21, s20, 31
	s_lshl_b64 s[20:21], s[20:21], 19
	s_add_u32 s54, s28, s20
	s_addc_u32 s55, s29, s21
	s_add_i32 s34, s12, 0
	s_add_i32 s35, s34, 0x10000
	s_mov_b32 m0, s35
	s_nop 0
	global_load_lds_dwordx4 v133, s[54:55]
	s_add_i32 s36, s34, 0x12000
	s_mov_b32 m0, s36
	s_nop 0
	global_load_lds_dwordx4 v135, s[54:55]
	s_add_u32 s20, s54, 0x40000
	s_addc_u32 s21, s55, 0
	s_add_i32 s37, s34, 0x14000
	s_mov_b32 m0, s37
	s_nop 0
	global_load_lds_dwordx4 v133, s[20:21]
	s_add_i32 s65, s34, 0x16000
	s_mov_b32 m0, s65
	s_nop 0
	global_load_lds_dwordx4 v135, s[20:21]
	s_add_u32 s56, s16, s22
	s_addc_u32 s57, s17, s23
	s_mov_b32 m0, s34
	s_nop 0
	global_load_lds_dwordx4 v220, s[56:57]
	s_add_i32 s66, s34, 0x2000
	s_mov_b32 m0, s66
	s_nop 0
	global_load_lds_dwordx4 v221, s[56:57]
	s_add_u32 s20, s56, 0x40000
	s_addc_u32 s21, s57, 0
	s_add_i32 s67, s34, 0x4000
	s_mov_b32 m0, s67
	s_nop 0
	global_load_lds_dwordx4 v222, s[20:21]
	s_add_i32 s68, s34, 0x6000
	s_mov_b32 m0, s68
	s_nop 0
	global_load_lds_dwordx4 v223, s[20:21]
	s_cmp_eq_u32 s10, 1
	s_cselect_b64 s[20:21], -1, 0
	s_cmp_lg_u32 s10, 1
	s_cbranch_scc1 .LBB0_1301
	s_barrier

.LBB0_1306:
	s_andn2_b64 vcc, exec, s[48:49]
	s_cbranch_vccnz .LBB0_1308
	s_ashr_i32 s10, s9, 31
	s_lshr_b32 s10, s10, 29
	s_add_i32 s10, s9, s10
	s_ashr_i32 s11, s10, 3
	s_and_b32 s10, s10, -8
	s_sub_i32 s9, s9, s10
	s_cmp_lt_i32 s9, 0
	s_cselect_b32 s10, s31, s30
	s_mul_i32 s9, s9, s10
	s_add_i32 s9, s9, s11
	s_mul_hi_i32 s10, s9, 0x92492493
	s_add_i32 s10, s10, s9
	s_lshr_b32 s11, s10, 31
	s_ashr_i32 s10, s10, 8
	s_add_i32 s10, s10, s11
	s_lshl_b32 s11, s10, 3
	s_sub_i32 s12, s27, s11
	s_min_i32 s12, s12, 8
	s_abs_i32 s42, s12
	v_cvt_f32_u32_e32 v0, s42
	s_sub_i32 s46, 0, s42
	s_mulk_i32 s10, 0x1c0
	s_sub_i32 s9, s9, s10
	v_rcp_iflag_f32_e32 v0, v0
	s_abs_i32 s10, s9
	s_xor_b32 s43, s9, s12
	s_ashr_i32 s43, s43, 31
	v_mul_f32_e32 v0, 0x4f7ffffe, v0
	v_cvt_u32_f32_e32 v0, v0
	s_nop 0
	v_readfirstlane_b32 s47, v0
	s_mul_i32 s46, s46, s47
	s_mul_hi_u32 s46, s47, s46
	s_add_i32 s47, s47, s46
	s_mul_hi_u32 s46, s10, s47
	s_mul_i32 s47, s46, s42
	s_sub_i32 s10, s10, s47
	s_add_i32 s48, s46, 1
	s_sub_i32 s47, s10, s42
	s_cmp_ge_u32 s10, s42
	s_cselect_b32 s46, s48, s46
	s_cselect_b32 s10, s47, s10
	s_add_i32 s47, s46, 1
	s_cmp_ge_u32 s10, s42
	s_cselect_b32 s10, s47, s46
	s_xor_b32 s10, s10, s43
	s_sub_i32 s84, s10, s43
	s_mul_i32 s10, s84, s12
	s_sub_i32 s9, s9, s10
	s_add_i32 s42, s11, s9
	s_ashr_i32 s43, s42, 31
	s_cmp_eq_u32 s42, s52
	s_cbranch_scc1 .Lgsk_b
	s_lshl_b64 s[10:11], s[42:43], 2
	s_add_u32 s10, s16, s10
	s_addc_u32 s11, s17, s11
	global_load_dword v0, v189, s[10:11] offset:768
	s_lshl_b32 s92, s42, 10
	s_add_u32 s10, s18, s92
	s_addc_u32 s11, s19, 0
	global_load_dword v224, v232, s[10:11]
	global_load_dword v225, v233, s[10:11]
	global_load_dword v226, v232, s[10:11] offset:512
	global_load_dword v227, v233, s[10:11] offset:512
	s_waitcnt vmcnt(0)
	s_lshl_b32 s92, s42, 19
	v_lshl_add_u32 v224, v224, 11, v234
	v_lshl_add_u32 v225, v225, 11, v235
	v_lshl_add_u32 v226, v226, 11, v234
	v_lshl_add_u32 v227, v227, 11, v235
	v_subrev_u32_e32 v224, s92, v224
	v_subrev_u32_e32 v225, s92, v225
	s_add_i32 s92, s92, 0x40000
	v_subrev_u32_e32 v226, s92, v226
	v_subrev_u32_e32 v227, s92, v227
	v_readfirstlane_b32 s9, v0
	s_mul_i32 s9, s9, 56
	s_mov_b32 s94, s9
	s_branch .Lgsk_c
.Lgsk_b:
	s_waitcnt vmcnt(0)
	v_mov_b32_e32 v224, v220
	v_mov_b32_e32 v225, v221
	v_mov_b32_e32 v226, v222
	v_mov_b32_e32 v227, v223
	s_mov_b32 s9, s94
.Lgsk_c:
	s_add_i32 s46, s9, s84
